# waves 4-7 take the per-tile barrier in front of the last two QK^T slices (all their K-fragment reads are complete there) and sleep before the softmax
# speedup vs baseline: 1.0162x; 1.0037x over previous
.LBB0_557:
	ds_read_b64_tr_b16 v[144:145], v177 offset:0
	ds_read_b64_tr_b16 v[146:147], v177 offset:0x1000
	ds_read_b64_tr_b16 v[148:149], v177 offset:0x2000
	ds_read_b64_tr_b16 v[150:151], v177 offset:0x3000
	ds_read_b64_tr_b16 v[152:153], v177 offset:0x4000
	ds_read_b64_tr_b16 v[154:155], v177 offset:0x5000
	ds_read_b64_tr_b16 v[156:157], v177 offset:0x6000
	ds_read_b64_tr_b16 v[158:159], v177 offset:0x7000
	s_waitcnt lgkmcnt(6)
	s_nop 0
	v_mfma_f32_32x32x16_bf16 v[112:127], v[144:147], v[128:131], v[112:127]
	ds_read_b64_tr_b16 v[192:193], v177 offset:0x200
	ds_read_b64_tr_b16 v[194:195], v177 offset:0x1200
	s_waitcnt lgkmcnt(6)
	v_mfma_f32_32x32x16_bf16 v[112:127], v[148:151], v[132:135], v[112:127]
	ds_read_b64_tr_b16 v[196:197], v177 offset:0x2200
	ds_read_b64_tr_b16 v[198:199], v177 offset:0x3200
	s_waitcnt lgkmcnt(6)
	v_mfma_f32_32x32x16_bf16 v[112:127], v[152:155], v[136:139], v[112:127]
	ds_read_b64_tr_b16 v[200:201], v177 offset:0x4200
	ds_read_b64_tr_b16 v[202:203], v177 offset:0x5200
	s_waitcnt lgkmcnt(6)
	v_mfma_f32_32x32x16_bf16 v[112:127], v[156:159], v[140:143], v[112:127]
	ds_read_b64_tr_b16 v[204:205], v177 offset:0x6200
	ds_read_b64_tr_b16 v[206:207], v177 offset:0x7200
	s_waitcnt lgkmcnt(6)
	v_mfma_f32_32x32x16_bf16 v[80:95], v[192:195], v[128:131], v[80:95]
	ds_read_b64_tr_b16 v[144:145], v177 offset:0x400
	ds_read_b64_tr_b16 v[146:147], v177 offset:0x1400
	s_waitcnt lgkmcnt(6)
	v_mfma_f32_32x32x16_bf16 v[80:95], v[196:199], v[132:135], v[80:95]
	ds_read_b64_tr_b16 v[148:149], v177 offset:0x2400
	ds_read_b64_tr_b16 v[150:151], v177 offset:0x3400
	s_waitcnt lgkmcnt(6)
	v_mfma_f32_32x32x16_bf16 v[80:95], v[200:203], v[136:139], v[80:95]
	ds_read_b64_tr_b16 v[152:153], v177 offset:0x4400
	ds_read_b64_tr_b16 v[154:155], v177 offset:0x5400
	s_waitcnt lgkmcnt(6)
	v_mfma_f32_32x32x16_bf16 v[80:95], v[204:207], v[140:143], v[80:95]
	ds_read_b64_tr_b16 v[156:157], v177 offset:0x6400
	ds_read_b64_tr_b16 v[158:159], v177 offset:0x7400
	s_waitcnt lgkmcnt(6)
	v_mfma_f32_32x32x16_bf16 v[96:111], v[144:147], v[128:131], v[96:111]
	ds_read_b64_tr_b16 v[192:193], v177 offset:0x600
	ds_read_b64_tr_b16 v[194:195], v177 offset:0x1600
	s_waitcnt lgkmcnt(6)
	v_mfma_f32_32x32x16_bf16 v[96:111], v[148:151], v[132:135], v[96:111]
	ds_read_b64_tr_b16 v[196:197], v177 offset:0x2600
	ds_read_b64_tr_b16 v[198:199], v177 offset:0x3600
	s_waitcnt lgkmcnt(6)
	v_mfma_f32_32x32x16_bf16 v[96:111], v[152:155], v[136:139], v[96:111]
	ds_read_b64_tr_b16 v[200:201], v177 offset:0x4600
	ds_read_b64_tr_b16 v[202:203], v177 offset:0x5600
	s_waitcnt lgkmcnt(6)
	v_mfma_f32_32x32x16_bf16 v[96:111], v[156:159], v[140:143], v[96:111]
	ds_read_b64_tr_b16 v[204:205], v177 offset:0x6600
	ds_read_b64_tr_b16 v[206:207], v177 offset:0x7600
	s_waitcnt lgkmcnt(6)
	v_mfma_f32_32x32x16_bf16 v[64:79], v[192:195], v[128:131], v[64:79]
	ds_read_b64_tr_b16 v[144:145], v177 offset:0x800
	ds_read_b64_tr_b16 v[146:147], v177 offset:0x1800
	s_waitcnt lgkmcnt(6)
	v_mfma_f32_32x32x16_bf16 v[64:79], v[196:199], v[132:135], v[64:79]
	ds_read_b64_tr_b16 v[148:149], v177 offset:0x2800
	ds_read_b64_tr_b16 v[150:151], v177 offset:0x3800
	s_waitcnt lgkmcnt(6)
	v_mfma_f32_32x32x16_bf16 v[64:79], v[200:203], v[136:139], v[64:79]
	ds_read_b64_tr_b16 v[152:153], v177 offset:0x4800
	ds_read_b64_tr_b16 v[154:155], v177 offset:0x5800
	s_waitcnt lgkmcnt(6)
	v_mfma_f32_32x32x16_bf16 v[64:79], v[204:207], v[140:143], v[64:79]
	ds_read_b64_tr_b16 v[156:157], v177 offset:0x6800
	ds_read_b64_tr_b16 v[158:159], v177 offset:0x7800
	s_waitcnt lgkmcnt(6)
	v_mfma_f32_32x32x16_bf16 v[48:63], v[144:147], v[128:131], v[48:63]
	ds_read_b64_tr_b16 v[192:193], v177 offset:0xa00
	ds_read_b64_tr_b16 v[194:195], v177 offset:0x1a00
	s_waitcnt lgkmcnt(6)
	v_mfma_f32_32x32x16_bf16 v[48:63], v[148:151], v[132:135], v[48:63]
	ds_read_b64_tr_b16 v[196:197], v177 offset:0x2a00
	ds_read_b64_tr_b16 v[198:199], v177 offset:0x3a00
	s_waitcnt lgkmcnt(6)
	v_mfma_f32_32x32x16_bf16 v[48:63], v[152:155], v[136:139], v[48:63]
	ds_read_b64_tr_b16 v[200:201], v177 offset:0x4a00
	ds_read_b64_tr_b16 v[202:203], v177 offset:0x5a00
	s_waitcnt lgkmcnt(6)
	v_mfma_f32_32x32x16_bf16 v[48:63], v[156:159], v[140:143], v[48:63]
	ds_read_b64_tr_b16 v[204:205], v177 offset:0x6a00
	ds_read_b64_tr_b16 v[206:207], v177 offset:0x7a00
	s_waitcnt lgkmcnt(6)
	v_mfma_f32_32x32x16_bf16 v[32:47], v[192:195], v[128:131], v[32:47]
	ds_read_b64_tr_b16 v[144:145], v177 offset:0xc00
	ds_read_b64_tr_b16 v[146:147], v177 offset:0x1c00
	s_waitcnt lgkmcnt(6)
	v_mfma_f32_32x32x16_bf16 v[32:47], v[196:199], v[132:135], v[32:47]
	ds_read_b64_tr_b16 v[148:149], v177 offset:0x2c00
	ds_read_b64_tr_b16 v[150:151], v177 offset:0x3c00
	s_waitcnt lgkmcnt(6)
	v_mfma_f32_32x32x16_bf16 v[32:47], v[200:203], v[136:139], v[32:47]
	ds_read_b64_tr_b16 v[152:153], v177 offset:0x4c00
	ds_read_b64_tr_b16 v[154:155], v177 offset:0x5c00
	s_waitcnt lgkmcnt(6)
	v_mfma_f32_32x32x16_bf16 v[32:47], v[204:207], v[140:143], v[32:47]
	ds_read_b64_tr_b16 v[156:157], v177 offset:0x6c00
	ds_read_b64_tr_b16 v[158:159], v177 offset:0x7c00
	s_waitcnt lgkmcnt(6)
	v_mfma_f32_32x32x16_bf16 v[16:31], v[144:147], v[128:131], v[16:31]
	ds_read_b64_tr_b16 v[192:193], v177 offset:0xe00
	ds_read_b64_tr_b16 v[194:195], v177 offset:0x1e00
	s_waitcnt lgkmcnt(6)
	v_mfma_f32_32x32x16_bf16 v[16:31], v[148:151], v[132:135], v[16:31]
	ds_read_b64_tr_b16 v[196:197], v177 offset:0x2e00
	ds_read_b64_tr_b16 v[198:199], v177 offset:0x3e00
	s_waitcnt lgkmcnt(6)
	v_mfma_f32_32x32x16_bf16 v[16:31], v[152:155], v[136:139], v[16:31]
	ds_read_b64_tr_b16 v[200:201], v177 offset:0x4e00
	ds_read_b64_tr_b16 v[202:203], v177 offset:0x5e00
	s_waitcnt lgkmcnt(6)
	v_mfma_f32_32x32x16_bf16 v[16:31], v[156:159], v[140:143], v[16:31]
	ds_read_b64_tr_b16 v[204:205], v177 offset:0x6e00
	ds_read_b64_tr_b16 v[206:207], v177 offset:0x7e00
	s_waitcnt lgkmcnt(6)
	v_mfma_f32_32x32x16_bf16 v[0:15], v[192:195], v[128:131], v[0:15]
	ds_read_b128 v[236:239], v188 offset:0
	ds_read_b128 v[240:243], v188 offset:0x2000
	s_waitcnt lgkmcnt(6)
	v_mfma_f32_32x32x16_bf16 v[0:15], v[196:199], v[132:135], v[0:15]
	ds_read_b128 v[244:247], v180 offset:0
	ds_read_b128 v[248:251], v187 offset:0
	s_waitcnt lgkmcnt(6)
	v_mfma_f32_32x32x16_bf16 v[0:15], v[200:203], v[136:139], v[0:15]
	ds_read_b128 v[218:221], v187 offset:0x2000
	ds_read_b128 v[222:225], v180 offset:0x400
	s_waitcnt lgkmcnt(6)
	v_mfma_f32_32x32x16_bf16 v[0:15], v[204:207], v[140:143], v[0:15]
	s_waitcnt lgkmcnt(3)
	s_nop 0
	v_mfma_f32_32x32x16_bf16 v[144:159], v[236:239], v[244:247], 0
	ds_read_b128 v[192:195], v186 offset:0
	ds_read_b128 v[196:199], v186 offset:0x2000
	v_mfma_f32_32x32x16_bf16 v[128:143], v[240:243], v[244:247], 0
	ds_read_b128 v[200:203], v180 offset:0x800
	s_waitcnt lgkmcnt(3)
	v_mfma_f32_32x32x16_bf16 v[144:159], v[248:251], v[222:225], v[144:159]
	ds_read_b128 v[236:239], v185 offset:0
	ds_read_b128 v[240:243], v185 offset:0x2000
	v_mfma_f32_32x32x16_bf16 v[128:143], v[218:221], v[222:225], v[128:143]
	ds_read_b128 v[244:247], v180 offset:0xc00
	s_waitcnt lgkmcnt(3)
	v_mfma_f32_32x32x16_bf16 v[144:159], v[192:195], v[200:203], v[144:159]
	ds_read_b128 v[248:251], v188 offset:0x80
	ds_read_b128 v[218:221], v188 offset:0x2080
	v_mfma_f32_32x32x16_bf16 v[128:143], v[196:199], v[200:203], v[128:143]
	ds_read_b128 v[222:225], v180 offset:0x1000
	s_waitcnt lgkmcnt(3)
	v_mfma_f32_32x32x16_bf16 v[144:159], v[236:239], v[244:247], v[144:159]
	ds_read_b128 v[192:195], v187 offset:0x80
	ds_read_b128 v[196:199], v187 offset:0x2080
	v_mfma_f32_32x32x16_bf16 v[128:143], v[240:243], v[244:247], v[128:143]
	ds_read_b128 v[200:203], v180 offset:0x1400
	s_waitcnt lgkmcnt(3)
	v_mfma_f32_32x32x16_bf16 v[144:159], v[248:251], v[222:225], v[144:159]
	ds_read_b128 v[236:239], v186 offset:0x80
	ds_read_b128 v[240:243], v186 offset:0x2080
	v_mfma_f32_32x32x16_bf16 v[128:143], v[218:221], v[222:225], v[128:143]
	ds_read_b128 v[244:247], v180 offset:0x1800
	s_waitcnt lgkmcnt(3)
	v_mfma_f32_32x32x16_bf16 v[144:159], v[192:195], v[200:203], v[144:159]
	ds_read_b128 v[248:251], v185 offset:0x80
	ds_read_b128 v[218:221], v185 offset:0x2080
	v_mfma_f32_32x32x16_bf16 v[128:143], v[196:199], v[200:203], v[128:143]
	s_bitcmp0_b32 s100, 8
	s_cbranch_scc1 .Lqkbar_m0_1
	s_waitcnt vmcnt(0)
	s_waitcnt lgkmcnt(0)
	s_barrier
.Lqkbar_m0_1:
	s_waitcnt lgkmcnt(2)
	v_mfma_f32_32x32x16_bf16 v[144:159], v[236:239], v[244:247], v[144:159]
	v_mfma_f32_32x32x16_bf16 v[128:143], v[240:243], v[244:247], v[128:143]
	s_waitcnt lgkmcnt(0)
	v_mfma_f32_32x32x16_bf16 v[144:159], v[248:251], v[166:169], v[144:159]
	v_mfma_f32_32x32x16_bf16 v[128:143], v[218:221], v[166:169], v[128:143]
	s_bitcmp0_b32 s100, 8
	s_cbranch_scc1 .Lstg_a10
	s_sleep 5

.LBB0_565:
	ds_read_b64_tr_b16 v[144:145], v177 offset:0x8000
	ds_read_b64_tr_b16 v[146:147], v177 offset:0x9000
	ds_read_b64_tr_b16 v[148:149], v177 offset:0xa000
	ds_read_b64_tr_b16 v[150:151], v177 offset:0xb000
	ds_read_b64_tr_b16 v[152:153], v177 offset:0xc000
	ds_read_b64_tr_b16 v[154:155], v177 offset:0xd000
	ds_read_b64_tr_b16 v[156:157], v177 offset:0xe000
	ds_read_b64_tr_b16 v[158:159], v177 offset:0xf000
	s_waitcnt lgkmcnt(6)
	s_nop 0
	v_mfma_f32_32x32x16_bf16 v[112:127], v[144:147], v[128:131], v[112:127]
	ds_read_b64_tr_b16 v[194:195], v177 offset:0x8200
	ds_read_b64_tr_b16 v[196:197], v177 offset:0x9200
	s_waitcnt lgkmcnt(6)
	v_mfma_f32_32x32x16_bf16 v[112:127], v[148:151], v[132:135], v[112:127]
	ds_read_b64_tr_b16 v[198:199], v177 offset:0xa200
	ds_read_b64_tr_b16 v[200:201], v177 offset:0xb200
	s_waitcnt lgkmcnt(6)
	v_mfma_f32_32x32x16_bf16 v[112:127], v[152:155], v[136:139], v[112:127]
	ds_read_b64_tr_b16 v[202:203], v177 offset:0xc200
	ds_read_b64_tr_b16 v[204:205], v177 offset:0xd200
	s_waitcnt lgkmcnt(6)
	v_mfma_f32_32x32x16_bf16 v[112:127], v[156:159], v[140:143], v[112:127]
	ds_read_b64_tr_b16 v[206:207], v177 offset:0xe200
	ds_read_b64_tr_b16 v[208:209], v177 offset:0xf200
	s_waitcnt lgkmcnt(6)
	v_mfma_f32_32x32x16_bf16 v[80:95], v[194:197], v[128:131], v[80:95]
	ds_read_b64_tr_b16 v[144:145], v177 offset:0x8400
	ds_read_b64_tr_b16 v[146:147], v177 offset:0x9400
	s_waitcnt lgkmcnt(6)
	v_mfma_f32_32x32x16_bf16 v[80:95], v[198:201], v[132:135], v[80:95]
	ds_read_b64_tr_b16 v[148:149], v177 offset:0xa400
	ds_read_b64_tr_b16 v[150:151], v177 offset:0xb400
	s_waitcnt lgkmcnt(6)
	v_mfma_f32_32x32x16_bf16 v[80:95], v[202:205], v[136:139], v[80:95]
	ds_read_b64_tr_b16 v[152:153], v177 offset:0xc400
	ds_read_b64_tr_b16 v[154:155], v177 offset:0xd400
	s_waitcnt lgkmcnt(6)
	v_mfma_f32_32x32x16_bf16 v[80:95], v[206:209], v[140:143], v[80:95]
	ds_read_b64_tr_b16 v[156:157], v177 offset:0xe400
	ds_read_b64_tr_b16 v[158:159], v177 offset:0xf400
	s_waitcnt lgkmcnt(6)
	v_mfma_f32_32x32x16_bf16 v[96:111], v[144:147], v[128:131], v[96:111]
	ds_read_b64_tr_b16 v[194:195], v177 offset:0x8600
	ds_read_b64_tr_b16 v[196:197], v177 offset:0x9600
	s_waitcnt lgkmcnt(6)
	v_mfma_f32_32x32x16_bf16 v[96:111], v[148:151], v[132:135], v[96:111]
	ds_read_b64_tr_b16 v[198:199], v177 offset:0xa600
	ds_read_b64_tr_b16 v[200:201], v177 offset:0xb600
	s_waitcnt lgkmcnt(6)
	v_mfma_f32_32x32x16_bf16 v[96:111], v[152:155], v[136:139], v[96:111]
	ds_read_b64_tr_b16 v[202:203], v177 offset:0xc600
	ds_read_b64_tr_b16 v[204:205], v177 offset:0xd600
	s_waitcnt lgkmcnt(6)
	v_mfma_f32_32x32x16_bf16 v[96:111], v[156:159], v[140:143], v[96:111]
	ds_read_b64_tr_b16 v[206:207], v177 offset:0xe600
	ds_read_b64_tr_b16 v[208:209], v177 offset:0xf600
	s_waitcnt lgkmcnt(6)
	v_mfma_f32_32x32x16_bf16 v[64:79], v[194:197], v[128:131], v[64:79]
	ds_read_b64_tr_b16 v[144:145], v177 offset:0x8800
	ds_read_b64_tr_b16 v[146:147], v177 offset:0x9800
	s_waitcnt lgkmcnt(6)
	v_mfma_f32_32x32x16_bf16 v[64:79], v[198:201], v[132:135], v[64:79]
	ds_read_b64_tr_b16 v[148:149], v177 offset:0xa800
	ds_read_b64_tr_b16 v[150:151], v177 offset:0xb800
	s_waitcnt lgkmcnt(6)
	v_mfma_f32_32x32x16_bf16 v[64:79], v[202:205], v[136:139], v[64:79]
	ds_read_b64_tr_b16 v[152:153], v177 offset:0xc800
	ds_read_b64_tr_b16 v[154:155], v177 offset:0xd800
	s_waitcnt lgkmcnt(6)
	v_mfma_f32_32x32x16_bf16 v[64:79], v[206:209], v[140:143], v[64:79]
	ds_read_b64_tr_b16 v[156:157], v177 offset:0xe800
	ds_read_b64_tr_b16 v[158:159], v177 offset:0xf800
	s_waitcnt lgkmcnt(6)
	v_mfma_f32_32x32x16_bf16 v[48:63], v[144:147], v[128:131], v[48:63]
	ds_read_b64_tr_b16 v[194:195], v177 offset:0x8a00
	ds_read_b64_tr_b16 v[196:197], v177 offset:0x9a00
	s_waitcnt lgkmcnt(6)
	v_mfma_f32_32x32x16_bf16 v[48:63], v[148:151], v[132:135], v[48:63]
	ds_read_b64_tr_b16 v[198:199], v177 offset:0xaa00
	ds_read_b64_tr_b16 v[200:201], v177 offset:0xba00
	s_waitcnt lgkmcnt(6)
	v_mfma_f32_32x32x16_bf16 v[48:63], v[152:155], v[136:139], v[48:63]
	ds_read_b64_tr_b16 v[202:203], v177 offset:0xca00
	ds_read_b64_tr_b16 v[204:205], v177 offset:0xda00
	s_waitcnt lgkmcnt(6)
	v_mfma_f32_32x32x16_bf16 v[48:63], v[156:159], v[140:143], v[48:63]
	ds_read_b64_tr_b16 v[206:207], v177 offset:0xea00
	ds_read_b64_tr_b16 v[208:209], v177 offset:0xfa00
	s_waitcnt lgkmcnt(6)
	v_mfma_f32_32x32x16_bf16 v[32:47], v[194:197], v[128:131], v[32:47]
	ds_read_b64_tr_b16 v[144:145], v177 offset:0x8c00
	ds_read_b64_tr_b16 v[146:147], v177 offset:0x9c00
	s_waitcnt lgkmcnt(6)
	v_mfma_f32_32x32x16_bf16 v[32:47], v[198:201], v[132:135], v[32:47]
	ds_read_b64_tr_b16 v[148:149], v177 offset:0xac00
	ds_read_b64_tr_b16 v[150:151], v177 offset:0xbc00
	s_waitcnt lgkmcnt(6)
	v_mfma_f32_32x32x16_bf16 v[32:47], v[202:205], v[136:139], v[32:47]
	ds_read_b64_tr_b16 v[152:153], v177 offset:0xcc00
	ds_read_b64_tr_b16 v[154:155], v177 offset:0xdc00
	s_waitcnt lgkmcnt(6)
	v_mfma_f32_32x32x16_bf16 v[32:47], v[206:209], v[140:143], v[32:47]
	ds_read_b64_tr_b16 v[156:157], v177 offset:0xec00
	ds_read_b64_tr_b16 v[158:159], v177 offset:0xfc00
	s_waitcnt lgkmcnt(6)
	v_mfma_f32_32x32x16_bf16 v[16:31], v[144:147], v[128:131], v[16:31]
	ds_read_b64_tr_b16 v[194:195], v177 offset:0x8e00
	ds_read_b64_tr_b16 v[196:197], v177 offset:0x9e00
	s_waitcnt lgkmcnt(6)
	v_mfma_f32_32x32x16_bf16 v[16:31], v[148:151], v[132:135], v[16:31]
	ds_read_b64_tr_b16 v[198:199], v177 offset:0xae00
	ds_read_b64_tr_b16 v[200:201], v177 offset:0xbe00
	s_waitcnt lgkmcnt(6)
	v_mfma_f32_32x32x16_bf16 v[16:31], v[152:155], v[136:139], v[16:31]
	ds_read_b64_tr_b16 v[202:203], v177 offset:0xce00
	ds_read_b64_tr_b16 v[204:205], v177 offset:0xde00
	s_waitcnt lgkmcnt(6)
	v_mfma_f32_32x32x16_bf16 v[16:31], v[156:159], v[140:143], v[16:31]
	ds_read_b64_tr_b16 v[206:207], v177 offset:0xee00
	ds_read_b64_tr_b16 v[208:209], v177 offset:0xfe00
	s_waitcnt lgkmcnt(6)
	v_mfma_f32_32x32x16_bf16 v[0:15], v[194:197], v[128:131], v[0:15]
	ds_read_b128 v[236:239], v181 offset:0
	ds_read_b128 v[240:243], v181 offset:0x2000
	s_waitcnt lgkmcnt(6)
	v_mfma_f32_32x32x16_bf16 v[0:15], v[198:201], v[132:135], v[0:15]
	ds_read_b128 v[244:247], v180 offset:0
	ds_read_b128 v[248:251], v182 offset:0
	s_waitcnt lgkmcnt(6)
	v_mfma_f32_32x32x16_bf16 v[0:15], v[202:205], v[136:139], v[0:15]
	ds_read_b128 v[218:221], v182 offset:0x2000
	ds_read_b128 v[222:225], v180 offset:0x400
	s_waitcnt lgkmcnt(6)
	v_mfma_f32_32x32x16_bf16 v[0:15], v[206:209], v[140:143], v[0:15]
	s_waitcnt lgkmcnt(3)
	s_nop 0
	v_mfma_f32_32x32x16_bf16 v[144:159], v[236:239], v[244:247], 0
	ds_read_b128 v[194:197], v183 offset:0
	ds_read_b128 v[198:201], v183 offset:0x2000
	v_mfma_f32_32x32x16_bf16 v[128:143], v[240:243], v[244:247], 0
	ds_read_b128 v[202:205], v180 offset:0x800
	s_waitcnt lgkmcnt(3)
	v_mfma_f32_32x32x16_bf16 v[144:159], v[248:251], v[222:225], v[144:159]
	ds_read_b128 v[236:239], v184 offset:0
	ds_read_b128 v[240:243], v184 offset:0x2000
	v_mfma_f32_32x32x16_bf16 v[128:143], v[218:221], v[222:225], v[128:143]
	ds_read_b128 v[244:247], v180 offset:0xc00
	s_waitcnt lgkmcnt(3)
	v_mfma_f32_32x32x16_bf16 v[144:159], v[194:197], v[202:205], v[144:159]
	ds_read_b128 v[248:251], v181 offset:0x80
	ds_read_b128 v[218:221], v181 offset:0x2080
	v_mfma_f32_32x32x16_bf16 v[128:143], v[198:201], v[202:205], v[128:143]
	ds_read_b128 v[222:225], v180 offset:0x1000
	s_waitcnt lgkmcnt(3)
	v_mfma_f32_32x32x16_bf16 v[144:159], v[236:239], v[244:247], v[144:159]
	ds_read_b128 v[194:197], v182 offset:0x80
	ds_read_b128 v[198:201], v182 offset:0x2080
	v_mfma_f32_32x32x16_bf16 v[128:143], v[240:243], v[244:247], v[128:143]
	ds_read_b128 v[202:205], v180 offset:0x1400
	s_waitcnt lgkmcnt(3)
	v_mfma_f32_32x32x16_bf16 v[144:159], v[248:251], v[222:225], v[144:159]
	ds_read_b128 v[236:239], v183 offset:0x80
	ds_read_b128 v[240:243], v183 offset:0x2080
	v_mfma_f32_32x32x16_bf16 v[128:143], v[218:221], v[222:225], v[128:143]
	ds_read_b128 v[244:247], v180 offset:0x1800
	s_waitcnt lgkmcnt(3)
	v_mfma_f32_32x32x16_bf16 v[144:159], v[194:197], v[202:205], v[144:159]
	ds_read_b128 v[248:251], v184 offset:0x80
	ds_read_b128 v[218:221], v184 offset:0x2080
	v_mfma_f32_32x32x16_bf16 v[128:143], v[198:201], v[202:205], v[128:143]
	s_bitcmp0_b32 s100, 8
	s_cbranch_scc1 .Lqkbar_m0_2
	s_waitcnt vmcnt(0)
	s_waitcnt lgkmcnt(0)
	s_barrier

.LBB0_589:
	ds_read_b64_tr_b16 v[144:145], v177 offset:0
	ds_read_b64_tr_b16 v[146:147], v177 offset:0x1000
	ds_read_b64_tr_b16 v[148:149], v177 offset:0x2000
	ds_read_b64_tr_b16 v[150:151], v177 offset:0x3000
	ds_read_b64_tr_b16 v[152:153], v177 offset:0x4000
	ds_read_b64_tr_b16 v[154:155], v177 offset:0x5000
	ds_read_b64_tr_b16 v[156:157], v177 offset:0x6000
	ds_read_b64_tr_b16 v[158:159], v177 offset:0x7000
	s_waitcnt lgkmcnt(6)
	s_nop 0
	v_mfma_f32_32x32x16_bf16 v[112:127], v[144:147], v[128:131], v[112:127]
	ds_read_b64_tr_b16 v[192:193], v177 offset:0x200
	ds_read_b64_tr_b16 v[194:195], v177 offset:0x1200
	s_waitcnt lgkmcnt(6)
	v_mfma_f32_32x32x16_bf16 v[112:127], v[148:151], v[132:135], v[112:127]
	ds_read_b64_tr_b16 v[196:197], v177 offset:0x2200
	ds_read_b64_tr_b16 v[198:199], v177 offset:0x3200
	s_waitcnt lgkmcnt(6)
	v_mfma_f32_32x32x16_bf16 v[112:127], v[152:155], v[136:139], v[112:127]
	ds_read_b64_tr_b16 v[200:201], v177 offset:0x4200
	ds_read_b64_tr_b16 v[202:203], v177 offset:0x5200
	s_waitcnt lgkmcnt(6)
	v_mfma_f32_32x32x16_bf16 v[112:127], v[156:159], v[140:143], v[112:127]
	ds_read_b64_tr_b16 v[204:205], v177 offset:0x6200
	ds_read_b64_tr_b16 v[206:207], v177 offset:0x7200
	s_waitcnt lgkmcnt(6)
	v_mfma_f32_32x32x16_bf16 v[96:111], v[192:195], v[128:131], v[96:111]
	ds_read_b64_tr_b16 v[144:145], v177 offset:0x400
	ds_read_b64_tr_b16 v[146:147], v177 offset:0x1400
	s_waitcnt lgkmcnt(6)
	v_mfma_f32_32x32x16_bf16 v[96:111], v[196:199], v[132:135], v[96:111]
	ds_read_b64_tr_b16 v[148:149], v177 offset:0x2400
	ds_read_b64_tr_b16 v[150:151], v177 offset:0x3400
	s_waitcnt lgkmcnt(6)
	v_mfma_f32_32x32x16_bf16 v[96:111], v[200:203], v[136:139], v[96:111]
	ds_read_b64_tr_b16 v[152:153], v177 offset:0x4400
	ds_read_b64_tr_b16 v[154:155], v177 offset:0x5400
	s_waitcnt lgkmcnt(6)
	v_mfma_f32_32x32x16_bf16 v[96:111], v[204:207], v[140:143], v[96:111]
	ds_read_b64_tr_b16 v[156:157], v177 offset:0x6400
	ds_read_b64_tr_b16 v[158:159], v177 offset:0x7400
	s_waitcnt lgkmcnt(6)
	v_mfma_f32_32x32x16_bf16 v[80:95], v[144:147], v[128:131], v[80:95]
	ds_read_b64_tr_b16 v[192:193], v177 offset:0x600
	ds_read_b64_tr_b16 v[194:195], v177 offset:0x1600
	s_waitcnt lgkmcnt(6)
	v_mfma_f32_32x32x16_bf16 v[80:95], v[148:151], v[132:135], v[80:95]
	ds_read_b64_tr_b16 v[196:197], v177 offset:0x2600
	ds_read_b64_tr_b16 v[198:199], v177 offset:0x3600
	s_waitcnt lgkmcnt(6)
	v_mfma_f32_32x32x16_bf16 v[80:95], v[152:155], v[136:139], v[80:95]
	ds_read_b64_tr_b16 v[200:201], v177 offset:0x4600
	ds_read_b64_tr_b16 v[202:203], v177 offset:0x5600
	s_waitcnt lgkmcnt(6)
	v_mfma_f32_32x32x16_bf16 v[80:95], v[156:159], v[140:143], v[80:95]
	ds_read_b64_tr_b16 v[204:205], v177 offset:0x6600
	ds_read_b64_tr_b16 v[206:207], v177 offset:0x7600
	s_waitcnt lgkmcnt(6)
	v_mfma_f32_32x32x16_bf16 v[64:79], v[192:195], v[128:131], v[64:79]
	ds_read_b64_tr_b16 v[144:145], v177 offset:0x800
	ds_read_b64_tr_b16 v[146:147], v177 offset:0x1800
	s_waitcnt lgkmcnt(6)
	v_mfma_f32_32x32x16_bf16 v[64:79], v[196:199], v[132:135], v[64:79]
	ds_read_b64_tr_b16 v[148:149], v177 offset:0x2800
	ds_read_b64_tr_b16 v[150:151], v177 offset:0x3800
	s_waitcnt lgkmcnt(6)
	v_mfma_f32_32x32x16_bf16 v[64:79], v[200:203], v[136:139], v[64:79]
	ds_read_b64_tr_b16 v[152:153], v177 offset:0x4800
	ds_read_b64_tr_b16 v[154:155], v177 offset:0x5800
	s_waitcnt lgkmcnt(6)
	v_mfma_f32_32x32x16_bf16 v[64:79], v[204:207], v[140:143], v[64:79]
	ds_read_b64_tr_b16 v[156:157], v177 offset:0x6800
	ds_read_b64_tr_b16 v[158:159], v177 offset:0x7800
	s_waitcnt lgkmcnt(6)
	v_mfma_f32_32x32x16_bf16 v[48:63], v[144:147], v[128:131], v[48:63]
	ds_read_b64_tr_b16 v[192:193], v177 offset:0xa00
	ds_read_b64_tr_b16 v[194:195], v177 offset:0x1a00
	s_waitcnt lgkmcnt(6)
	v_mfma_f32_32x32x16_bf16 v[48:63], v[148:151], v[132:135], v[48:63]
	ds_read_b64_tr_b16 v[196:197], v177 offset:0x2a00
	ds_read_b64_tr_b16 v[198:199], v177 offset:0x3a00
	s_waitcnt lgkmcnt(6)
	v_mfma_f32_32x32x16_bf16 v[48:63], v[152:155], v[136:139], v[48:63]
	ds_read_b64_tr_b16 v[200:201], v177 offset:0x4a00
	ds_read_b64_tr_b16 v[202:203], v177 offset:0x5a00
	s_waitcnt lgkmcnt(6)
	v_mfma_f32_32x32x16_bf16 v[48:63], v[156:159], v[140:143], v[48:63]
	ds_read_b64_tr_b16 v[204:205], v177 offset:0x6a00
	ds_read_b64_tr_b16 v[206:207], v177 offset:0x7a00
	s_waitcnt lgkmcnt(6)
	v_mfma_f32_32x32x16_bf16 v[32:47], v[192:195], v[128:131], v[32:47]
	ds_read_b64_tr_b16 v[144:145], v177 offset:0xc00
	ds_read_b64_tr_b16 v[146:147], v177 offset:0x1c00
	s_waitcnt lgkmcnt(6)
	v_mfma_f32_32x32x16_bf16 v[32:47], v[196:199], v[132:135], v[32:47]
	ds_read_b64_tr_b16 v[148:149], v177 offset:0x2c00
	ds_read_b64_tr_b16 v[150:151], v177 offset:0x3c00
	s_waitcnt lgkmcnt(6)
	v_mfma_f32_32x32x16_bf16 v[32:47], v[200:203], v[136:139], v[32:47]
	ds_read_b64_tr_b16 v[152:153], v177 offset:0x4c00
	ds_read_b64_tr_b16 v[154:155], v177 offset:0x5c00
	s_waitcnt lgkmcnt(6)
	v_mfma_f32_32x32x16_bf16 v[32:47], v[204:207], v[140:143], v[32:47]
	ds_read_b64_tr_b16 v[156:157], v177 offset:0x6c00
	ds_read_b64_tr_b16 v[158:159], v177 offset:0x7c00
	s_waitcnt lgkmcnt(6)
	v_mfma_f32_32x32x16_bf16 v[16:31], v[144:147], v[128:131], v[16:31]
	ds_read_b64_tr_b16 v[192:193], v177 offset:0xe00
	ds_read_b64_tr_b16 v[194:195], v177 offset:0x1e00
	s_waitcnt lgkmcnt(6)
	v_mfma_f32_32x32x16_bf16 v[16:31], v[148:151], v[132:135], v[16:31]
	ds_read_b64_tr_b16 v[196:197], v177 offset:0x2e00
	ds_read_b64_tr_b16 v[198:199], v177 offset:0x3e00
	s_waitcnt lgkmcnt(6)
	v_mfma_f32_32x32x16_bf16 v[16:31], v[152:155], v[136:139], v[16:31]
	ds_read_b64_tr_b16 v[200:201], v177 offset:0x4e00
	ds_read_b64_tr_b16 v[202:203], v177 offset:0x5e00
	s_waitcnt lgkmcnt(6)
	v_mfma_f32_32x32x16_bf16 v[16:31], v[156:159], v[140:143], v[16:31]
	ds_read_b64_tr_b16 v[204:205], v177 offset:0x6e00
	ds_read_b64_tr_b16 v[206:207], v177 offset:0x7e00
	s_waitcnt lgkmcnt(6)
	v_mfma_f32_32x32x16_bf16 v[0:15], v[192:195], v[128:131], v[0:15]
	ds_read_b128 v[236:239], v188 offset:0
	ds_read_b128 v[240:243], v188 offset:0x2000
	s_waitcnt lgkmcnt(6)
	v_mfma_f32_32x32x16_bf16 v[0:15], v[196:199], v[132:135], v[0:15]
	ds_read_b128 v[244:247], v180 offset:0
	ds_read_b128 v[248:251], v187 offset:0
	s_waitcnt lgkmcnt(6)
	v_mfma_f32_32x32x16_bf16 v[0:15], v[200:203], v[136:139], v[0:15]
	ds_read_b128 v[218:221], v187 offset:0x2000
	ds_read_b128 v[222:225], v180 offset:0x400
	s_waitcnt lgkmcnt(6)
	v_mfma_f32_32x32x16_bf16 v[0:15], v[204:207], v[140:143], v[0:15]
	s_waitcnt lgkmcnt(3)
	s_nop 0
	v_mfma_f32_32x32x16_bf16 v[144:159], v[236:239], v[244:247], 0
	ds_read_b128 v[192:195], v186 offset:0
	ds_read_b128 v[196:199], v186 offset:0x2000
	v_mfma_f32_32x32x16_bf16 v[128:143], v[240:243], v[244:247], 0
	ds_read_b128 v[200:203], v180 offset:0x800
	s_waitcnt lgkmcnt(3)
	v_mfma_f32_32x32x16_bf16 v[144:159], v[248:251], v[222:225], v[144:159]
	ds_read_b128 v[236:239], v185 offset:0
	ds_read_b128 v[240:243], v185 offset:0x2000
	v_mfma_f32_32x32x16_bf16 v[128:143], v[218:221], v[222:225], v[128:143]
	ds_read_b128 v[244:247], v180 offset:0xc00
	s_waitcnt lgkmcnt(3)
	v_mfma_f32_32x32x16_bf16 v[144:159], v[192:195], v[200:203], v[144:159]
	ds_read_b128 v[248:251], v188 offset:0x80
	ds_read_b128 v[218:221], v188 offset:0x2080
	v_mfma_f32_32x32x16_bf16 v[128:143], v[196:199], v[200:203], v[128:143]
	ds_read_b128 v[222:225], v180 offset:0x1000
	s_waitcnt lgkmcnt(3)
	v_mfma_f32_32x32x16_bf16 v[144:159], v[236:239], v[244:247], v[144:159]
	ds_read_b128 v[192:195], v187 offset:0x80
	ds_read_b128 v[196:199], v187 offset:0x2080
	v_mfma_f32_32x32x16_bf16 v[128:143], v[240:243], v[244:247], v[128:143]
	ds_read_b128 v[200:203], v180 offset:0x1400
	s_waitcnt lgkmcnt(3)
	v_mfma_f32_32x32x16_bf16 v[144:159], v[248:251], v[222:225], v[144:159]
	ds_read_b128 v[236:239], v186 offset:0x80
	ds_read_b128 v[240:243], v186 offset:0x2080
	v_mfma_f32_32x32x16_bf16 v[128:143], v[218:221], v[222:225], v[128:143]
	ds_read_b128 v[244:247], v180 offset:0x1800
	s_waitcnt lgkmcnt(3)
	v_mfma_f32_32x32x16_bf16 v[144:159], v[192:195], v[200:203], v[144:159]
	ds_read_b128 v[248:251], v185 offset:0x80
	ds_read_b128 v[218:221], v185 offset:0x2080
	v_mfma_f32_32x32x16_bf16 v[128:143], v[196:199], v[200:203], v[128:143]
	s_bitcmp0_b32 s100, 8
	s_cbranch_scc1 .Lqkbar_m1_3
	s_waitcnt vmcnt(0)
	s_waitcnt lgkmcnt(0)
	s_barrier

.LBB0_597:
	ds_read_b64_tr_b16 v[144:145], v177 offset:0x8000
	ds_read_b64_tr_b16 v[146:147], v177 offset:0x9000
	ds_read_b64_tr_b16 v[148:149], v177 offset:0xa000
	ds_read_b64_tr_b16 v[150:151], v177 offset:0xb000
	ds_read_b64_tr_b16 v[152:153], v177 offset:0xc000
	ds_read_b64_tr_b16 v[154:155], v177 offset:0xd000
	ds_read_b64_tr_b16 v[156:157], v177 offset:0xe000
	ds_read_b64_tr_b16 v[158:159], v177 offset:0xf000
	s_waitcnt lgkmcnt(6)
	s_nop 0
	v_mfma_f32_32x32x16_bf16 v[112:127], v[144:147], v[128:131], v[112:127]
	ds_read_b64_tr_b16 v[194:195], v177 offset:0x8200
	ds_read_b64_tr_b16 v[196:197], v177 offset:0x9200
	s_waitcnt lgkmcnt(6)
	v_mfma_f32_32x32x16_bf16 v[112:127], v[148:151], v[132:135], v[112:127]
	ds_read_b64_tr_b16 v[198:199], v177 offset:0xa200
	ds_read_b64_tr_b16 v[200:201], v177 offset:0xb200
	s_waitcnt lgkmcnt(6)
	v_mfma_f32_32x32x16_bf16 v[112:127], v[152:155], v[136:139], v[112:127]
	ds_read_b64_tr_b16 v[202:203], v177 offset:0xc200
	ds_read_b64_tr_b16 v[204:205], v177 offset:0xd200
	s_waitcnt lgkmcnt(6)
	v_mfma_f32_32x32x16_bf16 v[112:127], v[156:159], v[140:143], v[112:127]
	ds_read_b64_tr_b16 v[206:207], v177 offset:0xe200
	ds_read_b64_tr_b16 v[208:209], v177 offset:0xf200
	s_waitcnt lgkmcnt(6)
	v_mfma_f32_32x32x16_bf16 v[96:111], v[194:197], v[128:131], v[96:111]
	ds_read_b64_tr_b16 v[144:145], v177 offset:0x8400
	ds_read_b64_tr_b16 v[146:147], v177 offset:0x9400
	s_waitcnt lgkmcnt(6)
	v_mfma_f32_32x32x16_bf16 v[96:111], v[198:201], v[132:135], v[96:111]
	ds_read_b64_tr_b16 v[148:149], v177 offset:0xa400
	ds_read_b64_tr_b16 v[150:151], v177 offset:0xb400
	s_waitcnt lgkmcnt(6)
	v_mfma_f32_32x32x16_bf16 v[96:111], v[202:205], v[136:139], v[96:111]
	ds_read_b64_tr_b16 v[152:153], v177 offset:0xc400
	ds_read_b64_tr_b16 v[154:155], v177 offset:0xd400
	s_waitcnt lgkmcnt(6)
	v_mfma_f32_32x32x16_bf16 v[96:111], v[206:209], v[140:143], v[96:111]
	ds_read_b64_tr_b16 v[156:157], v177 offset:0xe400
	ds_read_b64_tr_b16 v[158:159], v177 offset:0xf400
	s_waitcnt lgkmcnt(6)
	v_mfma_f32_32x32x16_bf16 v[80:95], v[144:147], v[128:131], v[80:95]
	ds_read_b64_tr_b16 v[194:195], v177 offset:0x8600
	ds_read_b64_tr_b16 v[196:197], v177 offset:0x9600
	s_waitcnt lgkmcnt(6)
	v_mfma_f32_32x32x16_bf16 v[80:95], v[148:151], v[132:135], v[80:95]
	ds_read_b64_tr_b16 v[198:199], v177 offset:0xa600
	ds_read_b64_tr_b16 v[200:201], v177 offset:0xb600
	s_waitcnt lgkmcnt(6)
	v_mfma_f32_32x32x16_bf16 v[80:95], v[152:155], v[136:139], v[80:95]
	ds_read_b64_tr_b16 v[202:203], v177 offset:0xc600
	ds_read_b64_tr_b16 v[204:205], v177 offset:0xd600
	s_waitcnt lgkmcnt(6)
	v_mfma_f32_32x32x16_bf16 v[80:95], v[156:159], v[140:143], v[80:95]
	ds_read_b64_tr_b16 v[206:207], v177 offset:0xe600
	ds_read_b64_tr_b16 v[208:209], v177 offset:0xf600
	s_waitcnt lgkmcnt(6)
	v_mfma_f32_32x32x16_bf16 v[64:79], v[194:197], v[128:131], v[64:79]
	ds_read_b64_tr_b16 v[144:145], v177 offset:0x8800
	ds_read_b64_tr_b16 v[146:147], v177 offset:0x9800
	s_waitcnt lgkmcnt(6)
	v_mfma_f32_32x32x16_bf16 v[64:79], v[198:201], v[132:135], v[64:79]
	ds_read_b64_tr_b16 v[148:149], v177 offset:0xa800
	ds_read_b64_tr_b16 v[150:151], v177 offset:0xb800
	s_waitcnt lgkmcnt(6)
	v_mfma_f32_32x32x16_bf16 v[64:79], v[202:205], v[136:139], v[64:79]
	ds_read_b64_tr_b16 v[152:153], v177 offset:0xc800
	ds_read_b64_tr_b16 v[154:155], v177 offset:0xd800
	s_waitcnt lgkmcnt(6)
	v_mfma_f32_32x32x16_bf16 v[64:79], v[206:209], v[140:143], v[64:79]
	ds_read_b64_tr_b16 v[156:157], v177 offset:0xe800
	ds_read_b64_tr_b16 v[158:159], v177 offset:0xf800
	s_waitcnt lgkmcnt(6)
	v_mfma_f32_32x32x16_bf16 v[48:63], v[144:147], v[128:131], v[48:63]
	ds_read_b64_tr_b16 v[194:195], v177 offset:0x8a00
	ds_read_b64_tr_b16 v[196:197], v177 offset:0x9a00
	s_waitcnt lgkmcnt(6)
	v_mfma_f32_32x32x16_bf16 v[48:63], v[148:151], v[132:135], v[48:63]
	ds_read_b64_tr_b16 v[198:199], v177 offset:0xaa00
	ds_read_b64_tr_b16 v[200:201], v177 offset:0xba00
	s_waitcnt lgkmcnt(6)
	v_mfma_f32_32x32x16_bf16 v[48:63], v[152:155], v[136:139], v[48:63]
	ds_read_b64_tr_b16 v[202:203], v177 offset:0xca00
	ds_read_b64_tr_b16 v[204:205], v177 offset:0xda00
	s_waitcnt lgkmcnt(6)
	v_mfma_f32_32x32x16_bf16 v[48:63], v[156:159], v[140:143], v[48:63]
	ds_read_b64_tr_b16 v[206:207], v177 offset:0xea00
	ds_read_b64_tr_b16 v[208:209], v177 offset:0xfa00
	s_waitcnt lgkmcnt(6)
	v_mfma_f32_32x32x16_bf16 v[32:47], v[194:197], v[128:131], v[32:47]
	ds_read_b64_tr_b16 v[144:145], v177 offset:0x8c00
	ds_read_b64_tr_b16 v[146:147], v177 offset:0x9c00
	s_waitcnt lgkmcnt(6)
	v_mfma_f32_32x32x16_bf16 v[32:47], v[198:201], v[132:135], v[32:47]
	ds_read_b64_tr_b16 v[148:149], v177 offset:0xac00
	ds_read_b64_tr_b16 v[150:151], v177 offset:0xbc00
	s_waitcnt lgkmcnt(6)
	v_mfma_f32_32x32x16_bf16 v[32:47], v[202:205], v[136:139], v[32:47]
	ds_read_b64_tr_b16 v[152:153], v177 offset:0xcc00
	ds_read_b64_tr_b16 v[154:155], v177 offset:0xdc00
	s_waitcnt lgkmcnt(6)
	v_mfma_f32_32x32x16_bf16 v[32:47], v[206:209], v[140:143], v[32:47]
	ds_read_b64_tr_b16 v[156:157], v177 offset:0xec00
	ds_read_b64_tr_b16 v[158:159], v177 offset:0xfc00
	s_waitcnt lgkmcnt(6)
	v_mfma_f32_32x32x16_bf16 v[16:31], v[144:147], v[128:131], v[16:31]
	ds_read_b64_tr_b16 v[194:195], v177 offset:0x8e00
	ds_read_b64_tr_b16 v[196:197], v177 offset:0x9e00
	s_waitcnt lgkmcnt(6)
	v_mfma_f32_32x32x16_bf16 v[16:31], v[148:151], v[132:135], v[16:31]
	ds_read_b64_tr_b16 v[198:199], v177 offset:0xae00
	ds_read_b64_tr_b16 v[200:201], v177 offset:0xbe00
	s_waitcnt lgkmcnt(6)
	v_mfma_f32_32x32x16_bf16 v[16:31], v[152:155], v[136:139], v[16:31]
	ds_read_b64_tr_b16 v[202:203], v177 offset:0xce00
	ds_read_b64_tr_b16 v[204:205], v177 offset:0xde00
	s_waitcnt lgkmcnt(6)
	v_mfma_f32_32x32x16_bf16 v[16:31], v[156:159], v[140:143], v[16:31]
	ds_read_b64_tr_b16 v[206:207], v177 offset:0xee00
	ds_read_b64_tr_b16 v[208:209], v177 offset:0xfe00
	s_waitcnt lgkmcnt(6)
	v_mfma_f32_32x32x16_bf16 v[0:15], v[194:197], v[128:131], v[0:15]
	ds_read_b128 v[236:239], v181 offset:0
	ds_read_b128 v[240:243], v181 offset:0x2000
	s_waitcnt lgkmcnt(6)
	v_mfma_f32_32x32x16_bf16 v[0:15], v[198:201], v[132:135], v[0:15]
	ds_read_b128 v[244:247], v180 offset:0
	ds_read_b128 v[248:251], v182 offset:0
	s_waitcnt lgkmcnt(6)
	v_mfma_f32_32x32x16_bf16 v[0:15], v[202:205], v[136:139], v[0:15]
	ds_read_b128 v[218:221], v182 offset:0x2000
	ds_read_b128 v[222:225], v180 offset:0x400
	s_waitcnt lgkmcnt(6)
	v_mfma_f32_32x32x16_bf16 v[0:15], v[206:209], v[140:143], v[0:15]
	s_waitcnt lgkmcnt(3)
	s_nop 0
	v_mfma_f32_32x32x16_bf16 v[144:159], v[236:239], v[244:247], 0
	ds_read_b128 v[194:197], v183 offset:0
	ds_read_b128 v[198:201], v183 offset:0x2000
	v_mfma_f32_32x32x16_bf16 v[128:143], v[240:243], v[244:247], 0
	ds_read_b128 v[202:205], v180 offset:0x800
	s_waitcnt lgkmcnt(3)
	v_mfma_f32_32x32x16_bf16 v[144:159], v[248:251], v[222:225], v[144:159]
	ds_read_b128 v[236:239], v184 offset:0
	ds_read_b128 v[240:243], v184 offset:0x2000
	v_mfma_f32_32x32x16_bf16 v[128:143], v[218:221], v[222:225], v[128:143]
	ds_read_b128 v[244:247], v180 offset:0xc00
	s_waitcnt lgkmcnt(3)
	v_mfma_f32_32x32x16_bf16 v[144:159], v[194:197], v[202:205], v[144:159]
	ds_read_b128 v[248:251], v181 offset:0x80
	ds_read_b128 v[218:221], v181 offset:0x2080
	v_mfma_f32_32x32x16_bf16 v[128:143], v[198:201], v[202:205], v[128:143]
	ds_read_b128 v[222:225], v180 offset:0x1000
	s_waitcnt lgkmcnt(3)
	v_mfma_f32_32x32x16_bf16 v[144:159], v[236:239], v[244:247], v[144:159]
	ds_read_b128 v[194:197], v182 offset:0x80
	ds_read_b128 v[198:201], v182 offset:0x2080
	v_mfma_f32_32x32x16_bf16 v[128:143], v[240:243], v[244:247], v[128:143]
	ds_read_b128 v[202:205], v180 offset:0x1400
	s_waitcnt lgkmcnt(3)
	v_mfma_f32_32x32x16_bf16 v[144:159], v[248:251], v[222:225], v[144:159]
	ds_read_b128 v[236:239], v183 offset:0x80
	ds_read_b128 v[240:243], v183 offset:0x2080
	v_mfma_f32_32x32x16_bf16 v[128:143], v[218:221], v[222:225], v[128:143]
	ds_read_b128 v[244:247], v180 offset:0x1800
	s_waitcnt lgkmcnt(3)
	v_mfma_f32_32x32x16_bf16 v[144:159], v[194:197], v[202:205], v[144:159]
	ds_read_b128 v[248:251], v184 offset:0x80
	ds_read_b128 v[218:221], v184 offset:0x2080
	v_mfma_f32_32x32x16_bf16 v[128:143], v[198:201], v[202:205], v[128:143]
	s_bitcmp0_b32 s100, 8
	s_cbranch_scc1 .Lqkbar_m1_4
	s_waitcnt vmcnt(0)
	s_waitcnt lgkmcnt(0)
	s_barrier
